# rwkv step 1: the four late raw-row loads get their own destinations and go out with the other eleven (one round trip less per unit)
# speedup vs baseline: 1.1971x; 1.0018x over previous
.LBB0_391:
	s_ashr_i32 s0, s18, 5
	s_lshl_b32 s1, s0, 6
	s_add_i32 s8, s1, 0x7fffe000
	s_and_b32 s8, s8, 0x7fffff00
	s_addk_i32 s8, 0x2000
	s_and_b32 s9, s1, 0xfffff000
	s_cmpk_lt_i32 s0, 0x80
	v_mov_b32_e32 v103, v92
	s_cselect_b32 s0, s75, 0xc0
	s_movk_i32 s41, 0x1000
	s_cselect_b32 s8, s9, s8
	s_cselect_b32 s10, s41, 0x100
	s_and_b32 s0, s0, s1
	v_ashrrev_i32_e32 v142, 3, v103
	v_add_u32_e32 v2, s0, v142
	v_readlane_b32 s0, v255, 4
	v_readlane_b32 s1, v255, 5
	v_add_u32_e32 v96, s8, v2
	v_lshlrev_b32_e32 v3, 4, v103
	v_mov_b64_e32 v[0:1], s[0:1]
	s_movk_i32 s0, 0x2c00
	v_mad_i64_i32 v[0:1], s[0:1], v96, s0, v[0:1]
	v_and_b32_e32 v104, 0x70, v3
	v_lshl_add_u64 v[0:1], v[0:1], 0, v[104:105]
	s_mov_b64 s[0:1], 0x21301000
	v_lshl_add_u64 v[12:13], v[0:1], 0, s[0:1]
	s_lshl_b32 s28, s40, 7
	v_lshl_add_u64 v[14:15], v[12:13], 0, s[28:29]
	v_add_co_u32_e32 v0, vcc, s41, v14
	global_load_dwordx4 v[44:47], v[14:15], off offset:2048
	s_nop 0
	v_addc_co_u32_e32 v1, vcc, 0, v15, vcc
	global_load_dwordx4 v[28:31], v[0:1], off
	v_add_u32_e32 v0, 1, v2
	v_cmp_lt_i32_e64 s[8:9], 0, v2
	v_cmp_gt_i32_e64 s[10:11], s10, v0
	v_and_b32_e32 v137, 7, v103
	v_cndmask_b32_e64 v49, 0, -1, s[8:9]
	v_cndmask_b32_e64 v48, 0, v185, s[8:9]
	v_cndmask_b32_e64 v104, 0, v186, s[10:11]
	v_lshlrev_b32_e32 v56, 5, v137
	s_lshl_b32 s28, s26, 7
	v_lshl_add_u64 v[16:17], v[14:15], 0, v[48:49]
	v_lshl_add_u64 v[36:37], v[14:15], 0, v[104:105]
	v_add_u32_e32 v4, v112, v56
	v_add_u32_e32 v8, v115, v56
	s_mov_b64 s[12:13], 0x1000
	v_lshl_add_u64 v[40:41], v[12:13], 0, s[28:29]
	global_load_dwordx4 v[148:151], v[16:17], off offset:2048
	global_load_dwordx4 v[152:155], v[36:37], off offset:2048
	v_add_u32_e32 v57, v116, v56
	ds_read_b128 v[20:23], v4
	ds_read_b128 v[0:3], v4 offset:16
	ds_read_b128 v[24:27], v4 offset:256
	ds_read_b128 v[4:7], v4 offset:272
	ds_read_b128 v[80:83], v8
	ds_read_b128 v[72:75], v8 offset:16
	ds_read_b128 v[84:87], v8 offset:256
	ds_read_b128 v[76:79], v8 offset:272
	ds_read_b128 v[60:63], v57
	ds_read_b128 v[32:35], v57 offset:16
	s_lshl_b32 s0, s40, 8
	global_load_dwordx4 v[8:11], v[14:15], off
	v_lshl_add_u64 v[38:39], v[14:15], 0, s[12:13]
	global_load_dwordx4 v[16:19], v[16:17], off
	s_nop 0
	global_load_dwordx4 v[12:15], v[36:37], off
	s_mov_b64 s[12:13], 0x1800
	v_add_co_u32_e32 v36, vcc, s41, v40
	s_add_u32 s0, s7, s0
	v_lshl_add_u64 v[50:51], v[40:41], 0, s[12:13]
	v_addc_co_u32_e32 v37, vcc, 0, v41, vcc
	s_mov_b64 s[12:13], 0x1900
	v_lshl_add_u64 v[168:169], v[40:41], 0, s[12:13]
	s_addc_u32 s1, s4, 0
	v_lshl_add_u64 v[52:53], v[38:39], 0, v[48:49]
	v_lshl_add_u64 v[54:55], v[38:39], 0, v[104:105]
	global_load_dwordx4 v[40:43], v[36:37], off offset:2048
	global_load_dwordx4 v[64:67], v[52:53], off
	s_nop 0
	global_load_dwordx4 v[36:39], v[36:37], off offset:2304
	s_nop 0
	global_load_dwordx4 v[68:71], v[54:55], off
	global_load_dwordx4 v[156:159], v56, s[0:1] offset:16
	global_load_dwordx4 v[160:163], v56, s[0:1]
	v_lshl_add_u64 v[228:229], v[50:51], 0, v[48:49]
	global_load_dwordx4 v[216:219], v[228:229], off
	v_lshl_add_u64 v[228:229], v[50:51], 0, v[104:105]
	global_load_dwordx4 v[220:223], v[228:229], off
	v_lshl_add_u64 v[228:229], v[168:169], 0, v[48:49]
	global_load_dwordx4 v[224:227], v[228:229], off
	v_lshl_add_u64 v[228:229], v[168:169], 0, v[104:105]
	global_load_dwordx4 v[246:249], v[228:229], off
	ds_read_b128 v[164:167], v57 offset:256
	ds_read_b128 v[88:91], v57 offset:272
	s_cmp_eq_u32 s26, 0
	s_cselect_b64 s[12:13], -1, 0
	s_mov_b64 s[0:1], -1
	s_and_b64 vcc, exec, s[12:13]
	s_waitcnt vmcnt(16)
	v_lshlrev_b32_e32 v146, 16, v44
	v_and_b32_e32 v145, 0xffff0000, v44
	v_lshlrev_b32_e32 v144, 16, v45
	s_waitcnt vmcnt(15)
	v_lshlrev_b32_e32 v98, 16, v28
	v_and_b32_e32 v95, 0xffff0000, v28
	v_lshlrev_b32_e32 v100, 16, v29
	v_and_b32_e32 v99, 0xffff0000, v29
	v_and_b32_e32 v143, 0xffff0000, v45
	v_lshlrev_b32_e32 v141, 16, v46
	v_and_b32_e32 v140, 0xffff0000, v46
	v_lshlrev_b32_e32 v139, 16, v47
	v_and_b32_e32 v138, 0xffff0000, v47
	s_nop 0
	v_lshlrev_b32_e32 v102, 16, v30
	v_and_b32_e32 v101, 0xffff0000, v30
	s_waitcnt vmcnt(14)
	v_and_b32_e32 v30, 0xffff0000, v148
	v_lshlrev_b32_e32 v28, 16, v148
	s_and_b64 s[100:101], s[8:9], s[10:11]
	s_cmp_eq_u64 s[100:101], exec
	s_cbranch_scc1 .Lfp1
	v_cndmask_b32_e64 v30, 0, v30, s[8:9]
	s_waitcnt vmcnt(13)
	v_and_b32_e32 v97, 0xffff0000, v152
	v_cndmask_b32_e64 v28, 0, v28, s[8:9]
	v_lshlrev_b32_e32 v29, 16, v152
	v_cndmask_b32_e64 v97, 0, v97, s[10:11]
	v_sub_f32_e32 v30, v30, v145
	v_lshlrev_b32_e32 v104, 16, v149
	v_cndmask_b32_e64 v29, 0, v29, s[10:11]
	v_sub_f32_e32 v28, v28, v146
	v_sub_f32_e32 v97, v97, v145
	v_cndmask_b32_e64 v104, 0, v104, s[8:9]
	v_lshlrev_b32_e32 v147, 16, v153
	v_and_b32_e32 v148, 0xffff0000, v149
	s_waitcnt vmcnt(8)
	v_lshlrev_b32_e32 v170, 16, v64
	v_and_b32_e32 v64, 0xffff0000, v64
	v_cndmask_b32_e64 v64, 0, v64, s[8:9]
	v_sub_f32_e32 v172, v64, v95
	v_lshlrev_b32_e32 v64, 16, v65
	v_cndmask_b32_e64 v64, 0, v64, s[8:9]
	v_sub_f32_e32 v174, v64, v100
	v_and_b32_e32 v64, 0xffff0000, v65
	s_waitcnt vmcnt(6)
	v_and_b32_e32 v65, 0xffff0000, v69
	v_cndmask_b32_e64 v65, 0, v65, s[10:11]
	v_sub_f32_e32 v177, v65, v99
	v_lshlrev_b32_e32 v65, 16, v70
	v_cndmask_b32_e64 v65, 0, v65, s[10:11]
	v_sub_f32_e32 v179, v65, v102
	v_and_b32_e32 v65, 0xffff0000, v70
	v_cndmask_b32_e64 v65, 0, v65, s[10:11]
	v_cndmask_b32_e64 v64, 0, v64, s[8:9]
	v_sub_f32_e32 v181, v65, v101
	v_lshlrev_b32_e32 v65, 16, v71
	s_waitcnt lgkmcnt(7)
	v_fmac_f32_e32 v145, v30, v81
	v_lshlrev_b32_e32 v110, 16, v31
	v_sub_f32_e32 v29, v29, v146
	v_cndmask_b32_e64 v147, 0, v147, s[10:11]
	v_sub_f32_e32 v104, v104, v144
	v_cndmask_b32_e64 v148, 0, v148, s[8:9]
	v_and_b32_e32 v149, 0xffff0000, v153
	v_lshlrev_b32_e32 v152, 16, v150
	v_lshlrev_b32_e32 v171, 16, v68
	v_and_b32_e32 v68, 0xffff0000, v68
	v_sub_f32_e32 v176, v64, v99
	v_lshlrev_b32_e32 v64, 16, v66
	v_cndmask_b32_e64 v65, 0, v65, s[10:11]
	v_fmac_f32_e32 v146, v28, v80
	s_waitcnt lgkmcnt(5)
	v_fmac_f32_e32 v145, v97, v85
	v_sub_f32_e32 v147, v147, v144
	v_cndmask_b32_e64 v149, 0, v149, s[10:11]
	v_sub_f32_e32 v148, v148, v143
	v_cndmask_b32_e64 v152, 0, v152, s[8:9]
	v_lshlrev_b32_e32 v153, 16, v154
	v_and_b32_e32 v150, 0xffff0000, v150
	v_cndmask_b32_e64 v68, 0, v68, s[10:11]
	v_cndmask_b32_e64 v64, 0, v64, s[8:9]
	v_sub_f32_e32 v189, v65, v110
	v_fmac_f32_e32 v146, v29, v84
	v_fmac_f32_e32 v144, v104, v82
	s_waitcnt vmcnt(4)
	v_mul_f32_e32 v65, v161, v145
	v_sub_f32_e32 v149, v149, v143
	v_cndmask_b32_e64 v153, 0, v153, s[10:11]
	v_sub_f32_e32 v152, v152, v141
	v_cndmask_b32_e64 v150, 0, v150, s[8:9]
	v_and_b32_e32 v154, 0xffff0000, v154
	v_lshlrev_b32_e32 v168, 16, v151
	v_sub_f32_e32 v173, v68, v95
	v_lshlrev_b32_e32 v68, 16, v69
	v_sub_f32_e32 v178, v64, v102
	v_and_b32_e32 v64, 0xffff0000, v66
	v_fmac_f32_e32 v144, v147, v86
	v_fmac_f32_e32 v143, v148, v83
	v_mul_f32_e32 v66, v160, v146
	v_mul_f32_e32 v28, v65, v65
	v_sub_f32_e32 v153, v153, v141
	v_cndmask_b32_e64 v154, 0, v154, s[10:11]
	v_sub_f32_e32 v150, v150, v140
	v_cndmask_b32_e64 v168, 0, v168, s[8:9]
	v_lshlrev_b32_e32 v169, 16, v155
	v_and_b32_e32 v151, 0xffff0000, v151
	v_cndmask_b32_e64 v68, 0, v68, s[10:11]
	v_fmac_f32_e32 v143, v149, v87
	v_fmac_f32_e32 v141, v152, v72
	v_fmac_f32_e32 v28, v66, v66
	v_mul_f32_e32 v69, v162, v144
	v_sub_f32_e32 v154, v154, v140
	v_cndmask_b32_e64 v169, 0, v169, s[10:11]
	v_sub_f32_e32 v168, v168, v139
	v_cndmask_b32_e64 v151, 0, v151, s[8:9]
	v_and_b32_e32 v155, 0xffff0000, v155
	v_sub_f32_e32 v175, v68, v100
	s_waitcnt lgkmcnt(4)
	v_fmac_f32_e32 v141, v153, v76
	v_fmac_f32_e32 v140, v150, v73
	v_fmac_f32_e32 v28, v69, v69
	v_mul_f32_e32 v68, v163, v143
	v_sub_f32_e32 v169, v169, v139
	v_cndmask_b32_e64 v155, 0, v155, s[10:11]
	v_sub_f32_e32 v151, v151, v138
	v_cndmask_b32_e64 v64, 0, v64, s[8:9]
	v_fmac_f32_e32 v140, v154, v77
	v_fmac_f32_e32 v139, v168, v74
	v_fmac_f32_e32 v28, v68, v68
	v_mul_f32_e32 v72, v156, v141
	v_sub_f32_e32 v155, v155, v138
	v_sub_f32_e32 v180, v64, v101
	v_lshlrev_b32_e32 v64, 16, v67
	v_fmac_f32_e32 v139, v169, v78
	v_fmac_f32_e32 v138, v151, v75
	v_fmac_f32_e32 v28, v72, v72
	v_mul_f32_e32 v70, v157, v140
	v_cndmask_b32_e64 v64, 0, v64, s[8:9]
	v_fmac_f32_e32 v138, v155, v79
	v_fmac_f32_e32 v28, v70, v70
	v_mul_f32_e32 v73, v158, v139
	v_sub_f32_e32 v188, v64, v110
	v_fmac_f32_e32 v28, v73, v73
	v_mul_f32_e32 v64, v159, v138
	v_cndmask_b32_e64 v170, 0, v170, s[8:9]
	v_fmac_f32_e32 v28, v64, v64
	v_cndmask_b32_e64 v171, 0, v171, s[10:11]
	v_sub_f32_e32 v170, v170, v98
	v_add_f32_dpp v28, v28, v28 quad_perm:[1,0,3,2] row_mask:0xf bank_mask:0xf bound_ctrl:1
	v_sub_f32_e32 v171, v171, v98
	s_waitcnt lgkmcnt(3)
	v_fmac_f32_e32 v98, v170, v60
	v_fmac_f32_e32 v95, v172, v61
	v_fmac_f32_e32 v100, v174, v62
	v_fmac_f32_e32 v99, v176, v63
	s_waitcnt lgkmcnt(2)
	v_fmac_f32_e32 v102, v178, v32
	v_fmac_f32_e32 v101, v180, v33
	v_fmac_f32_e32 v110, v188, v34
	v_add_f32_dpp v62, v28, v28 quad_perm:[2,3,0,1] row_mask:0xf bank_mask:0xf bound_ctrl:1
	s_waitcnt lgkmcnt(1)
	v_fmac_f32_e32 v98, v171, v164
	v_fmac_f32_e32 v95, v173, v165
	v_mov_b32_dpp v63, v62 row_half_mirror row_mask:0xf bank_mask:0xf bound_ctrl:1
	v_fmac_f32_e32 v100, v175, v166
	v_fmac_f32_e32 v99, v177, v167
	s_waitcnt lgkmcnt(0)
	v_fmac_f32_e32 v102, v179, v88
	v_fmac_f32_e32 v101, v181, v89
	v_fmac_f32_e32 v110, v189, v90
	s_cbranch_vccnz .LBB0_393
	s_mov_b64 s[0:1], 0

.LBB0_395:
	s_waitcnt vmcnt(2)
	v_and_b32_e32 v33, 0xffff0000, v223
	v_and_b32_e32 v35, 0xffff0000, v219
	v_lshlrev_b32_e32 v34, 16, v38
	v_and_b32_e32 v32, 0xffff0000, v38
	v_lshlrev_b32_e32 v30, 16, v39
	v_and_b32_e32 v28, 0xffff0000, v39
	v_cndmask_b32_e64 v39, 0, v33, s[10:11]
	v_cndmask_b32_e64 v38, 0, v35, s[8:9]
	v_lshlrev_b32_e32 v33, 16, v216
	v_lshlrev_b32_e32 v35, 16, v220
	v_cndmask_b32_e64 v149, 0, v35, s[10:11]
	v_cndmask_b32_e64 v148, 0, v33, s[8:9]
	v_and_b32_e32 v33, 0xffff0000, v220
	v_and_b32_e32 v35, 0xffff0000, v216
	v_cndmask_b32_e64 v151, 0, v33, s[10:11]
	v_cndmask_b32_e64 v150, 0, v35, s[8:9]
	v_lshlrev_b32_e32 v33, 16, v217
	v_lshlrev_b32_e32 v35, 16, v221
	v_cndmask_b32_e64 v153, 0, v35, s[10:11]
	v_cndmask_b32_e64 v152, 0, v33, s[8:9]
	v_and_b32_e32 v33, 0xffff0000, v221
	v_and_b32_e32 v35, 0xffff0000, v217
	v_cndmask_b32_e64 v53, 0, v33, s[10:11]
	v_cndmask_b32_e64 v52, 0, v35, s[8:9]
	v_lshlrev_b32_e32 v33, 16, v218
	v_lshlrev_b32_e32 v35, 16, v222
	v_cndmask_b32_e64 v57, 0, v35, s[10:11]
	v_cndmask_b32_e64 v56, 0, v33, s[8:9]
	v_and_b32_e32 v33, 0xffff0000, v222
	v_and_b32_e32 v35, 0xffff0000, v218
	v_cndmask_b32_e64 v155, 0, v33, s[10:11]
	v_cndmask_b32_e64 v154, 0, v35, s[8:9]
	v_lshlrev_b32_e32 v33, 16, v219
	v_lshlrev_b32_e32 v35, 16, v223
	v_cndmask_b32_e64 v55, 0, v35, s[10:11]
	v_cndmask_b32_e64 v54, 0, v33, s[8:9]
	s_waitcnt vmcnt(1)
	v_lshlrev_b32_e32 v33, 16, v224
	s_waitcnt vmcnt(0)
	v_lshlrev_b32_e32 v35, 16, v246
	v_cndmask_b32_e64 v59, 0, v35, s[10:11]
	v_cndmask_b32_e64 v58, 0, v33, s[8:9]
	v_and_b32_e32 v33, 0xffff0000, v246
	v_and_b32_e32 v35, 0xffff0000, v224
	v_cndmask_b32_e64 v157, 0, v33, s[10:11]
	v_cndmask_b32_e64 v156, 0, v35, s[8:9]
	v_lshlrev_b32_e32 v33, 16, v225
	v_lshlrev_b32_e32 v35, 16, v247
	v_cndmask_b32_e64 v159, 0, v35, s[10:11]
	v_cndmask_b32_e64 v158, 0, v33, s[8:9]
	v_and_b32_e32 v33, 0xffff0000, v247
	v_and_b32_e32 v35, 0xffff0000, v225
	v_cndmask_b32_e64 v45, 0, v33, s[10:11]
	v_cndmask_b32_e64 v44, 0, v35, s[8:9]
	v_lshlrev_b32_e32 v33, 16, v226
	v_lshlrev_b32_e32 v35, 16, v248
	v_cndmask_b32_e64 v49, 0, v35, s[10:11]
	v_cndmask_b32_e64 v48, 0, v33, s[8:9]
	v_and_b32_e32 v33, 0xffff0000, v248
	v_and_b32_e32 v35, 0xffff0000, v226
	v_cndmask_b32_e64 v161, 0, v33, s[10:11]
	v_cndmask_b32_e64 v160, 0, v35, s[8:9]
	v_lshlrev_b32_e32 v33, 16, v227
	v_lshlrev_b32_e32 v35, 16, v249
	v_lshlrev_b32_e32 v67, 2, v74
	v_cndmask_b32_e64 v163, 0, v35, s[10:11]
	v_cndmask_b32_e64 v162, 0, v33, s[8:9]
	v_and_b32_e32 v33, 0xffff0000, v249
	v_and_b32_e32 v35, 0xffff0000, v227
	v_add_u32_e32 v29, v117, v67
	v_lshlrev_b32_e32 v84, 16, v42
	v_and_b32_e32 v86, 0xffff0000, v42
	v_lshlrev_b32_e32 v60, 16, v36
	v_and_b32_e32 v42, 0xffff0000, v36
	v_and_b32_e32 v36, 0xffff0000, v37
	v_cndmask_b32_e64 v47, 0, v33, s[10:11]
	v_cndmask_b32_e64 v46, 0, v35, s[8:9]

.Lfp1_395:
	s_waitcnt vmcnt(2)
	v_lshlrev_b32_e32 v34, 16, v38
	v_and_b32_e32 v32, 0xffff0000, v38
	v_lshlrev_b32_e32 v30, 16, v39
	v_and_b32_e32 v28, 0xffff0000, v39
	v_and_b32_e32 v39, 0xffff0000, v223
	v_and_b32_e32 v38, 0xffff0000, v219
	v_lshlrev_b32_e32 v149, 16, v220
	v_lshlrev_b32_e32 v148, 16, v216
	v_and_b32_e32 v151, 0xffff0000, v220
	v_and_b32_e32 v150, 0xffff0000, v216
	v_lshlrev_b32_e32 v153, 16, v221
	v_lshlrev_b32_e32 v152, 16, v217
	v_and_b32_e32 v53, 0xffff0000, v221
	v_and_b32_e32 v52, 0xffff0000, v217
	v_lshlrev_b32_e32 v57, 16, v222
	v_lshlrev_b32_e32 v56, 16, v218
	v_and_b32_e32 v155, 0xffff0000, v222
	v_and_b32_e32 v154, 0xffff0000, v218
	v_lshlrev_b32_e32 v55, 16, v223
	v_lshlrev_b32_e32 v54, 16, v219
	s_waitcnt vmcnt(1)
	s_waitcnt vmcnt(0)
	v_lshlrev_b32_e32 v59, 16, v246
	v_lshlrev_b32_e32 v58, 16, v224
	v_and_b32_e32 v157, 0xffff0000, v246
	v_and_b32_e32 v156, 0xffff0000, v224
	v_lshlrev_b32_e32 v159, 16, v247
	v_lshlrev_b32_e32 v158, 16, v225
	v_and_b32_e32 v45, 0xffff0000, v247
	v_and_b32_e32 v44, 0xffff0000, v225
	v_lshlrev_b32_e32 v49, 16, v248
	v_lshlrev_b32_e32 v48, 16, v226
	v_and_b32_e32 v161, 0xffff0000, v248
	v_and_b32_e32 v160, 0xffff0000, v226
	v_lshlrev_b32_e32 v67, 2, v74
	v_lshlrev_b32_e32 v163, 16, v249
	v_lshlrev_b32_e32 v162, 16, v227
	v_and_b32_e32 v33, 0xffff0000, v249
	v_and_b32_e32 v35, 0xffff0000, v227
	v_add_u32_e32 v29, v117, v67
	v_lshlrev_b32_e32 v84, 16, v42
	v_and_b32_e32 v86, 0xffff0000, v42
	v_lshlrev_b32_e32 v60, 16, v36
	v_and_b32_e32 v42, 0xffff0000, v36
	v_and_b32_e32 v36, 0xffff0000, v37
	v_cndmask_b32_e64 v47, 0, v33, s[10:11]
	v_cndmask_b32_e64 v46, 0, v35, s[8:9]
	s_branch .Lfp1_join
